# baseline (speedup 1.0000x reference)
_Z7k_fusedPKfS0_S0_S0_S0_S0_S0_S0_S0_S0_S0_S0_S0_S0_PfS1_:
	s_load_dwordx2 s[34:35], s[0:1], 0x70
	s_load_dwordx4 s[20:23], s[0:1], 0x60
	s_load_dwordx4 s[24:27], s[0:1], 0x40
	s_load_dwordx4 s[28:31], s[0:1], 0x10
	s_and_b32 s33, s2, 7
	s_ashr_i32 s36, s2, 3
	s_cmp_lt_i32 s36, 31
	s_mov_b64 s[2:3], -1
	s_cbranch_scc1 .LBB5_52
	s_endpgm
	s_mul_i32 s11, s33, 0x1cc8
	v_add_u32_e32 v1, s11, v0
	v_lshlrev_b32_e32 v22, 4, v1
	v_mov_b32_e32 v23, 0
	s_add_i32 s8, s11, 0x1cc8
	s_add_i32 s9, s11, 0x1a48
	s_add_i32 s10, s11, 0x17c8
	s_addk_i32 s11, 0x1548
	s_waitcnt lgkmcnt(0)
	v_lshl_add_u64 v[24:25], s[28:29], 0, v[22:23]
	s_mov_b64 s[2:3], 0
	s_mov_b64 s[4:5], 0xa000
	v_mov_b32_e32 v26, v1
	v_mov_b32_e32 v18, v23
	v_mov_b32_e32 v19, v23
	v_mov_b32_e32 v20, v23
	v_mov_b32_e32 v21, v23
	s_branch .LBB5_3

.LBB5_55:
	s_load_dwordx8 s[12:19], s[2:3], 0x4
	s_load_dword s49, s[2:3], 0x24
	s_add_u32 s42, s34, 0x125000
	s_addc_u32 s43, s35, 0
	v_lshlrev_b32_e32 v78, 4, v0
	global_load_dwordx4 v[2:5], v78, s[42:43]
	s_load_dwordx2 s[4:5], s[0:1], 0x28
	v_mov_b32_e32 v79, 0
	s_movk_i32 s6, 0x80
	v_lshl_add_u64 v[84:85], s[42:43], 0, v[78:79]
	v_cmp_gt_u32_e64 s[10:11], s6, v0
	s_and_saveexec_b64 s[6:7], s[10:11]
	s_cbranch_execz .LBB5_57
	v_add_co_u32_e32 v6, vcc, 0x2000, v84
	s_nop 1
	v_addc_co_u32_e32 v7, vcc, 0, v85, vcc
	global_load_dwordx4 v[6:9], v[6:7], off offset:2048
.LBB5_57:
	s_or_b64 exec, exec, s[6:7]
	v_cmp_gt_u32_e64 s[2:3], 64, v0
	v_mov_b32_e32 v86, 0x3e800000
	s_nop 0
	v_cndmask_b32_e64 v86, 1.0, v86, s[2:3]
	v_cmp_lt_u32_e32 vcc, 63, v0
	s_and_saveexec_b64 s[6:7], vcc
	s_xor_b64 s[6:7], exec, s[6:7]
	s_cbranch_execz .LBB5_61
	s_movk_i32 s38, 0x48
	v_cmp_gt_u32_e32 vcc, s38, v0
	v_mov_b32_e32 v1, 0
	s_and_saveexec_b64 s[38:39], vcc
	s_cbranch_execz .LBB5_60
	v_lshlrev_b32_e32 v10, 2, v0
	v_mov_b32_e32 v11, 0
	v_lshl_add_u64 v[10:11], s[34:35], 0, v[10:11]
	v_add_co_u32_e32 v10, vcc, 0xb000, v10
	s_nop 1
	v_addc_co_u32_e32 v11, vcc, 0, v11, vcc
	global_load_dword v1, v[10:11], off offset:3840

.LBB5_63:
	s_or_b64 exec, exec, s[6:7]
	s_movk_i32 s4, 0xff
	v_cmp_lt_u32_e32 vcc, s4, v0
	s_movk_i32 s4, 0x100
	v_and_b32_e32 v128, 63, v0
	v_cmp_gt_u32_e64 s[4:5], s4, v0
	v_mov_b32_e32 v14, 0
	s_and_saveexec_b64 s[38:39], s[4:5]
	s_cbranch_execz .LBB5_65
	s_load_dwordx4 s[52:55], s[0:1], 0x30
	s_movk_i32 s6, 0xc0
	v_cmp_gt_u32_e64 s[6:7], s6, v0
	s_waitcnt lgkmcnt(0)
	v_mov_b32_e32 v13, s54
	v_mov_b32_e32 v14, s52
	v_mov_b32_e32 v15, s55
	v_cndmask_b32_e64 v13, v13, v14, s[6:7]
	v_mov_b32_e32 v14, s53
	v_cndmask_b32_e64 v14, v15, v14, s[6:7]
	v_cndmask_b32_e64 v11, v14, v11, s[10:11]
	v_cndmask_b32_e64 v10, v13, v10, s[10:11]
	v_lshlrev_b32_e32 v14, 2, v128
	v_mov_b32_e32 v15, 0
	v_lshl_add_u64 v[10:11], v[10:11], 0, v[14:15]
	global_load_dword v14, v[10:11], off

.LBB5_73:
	s_or_b64 exec, exec, s[38:39]
	s_mul_i32 s38, s33, 0x133
	s_ashr_i32 s39, s37, 31
	s_add_u32 s40, s37, s38
	s_addc_u32 s39, s39, 0
	s_mulk_i32 s39, 0xc00
	s_mul_hi_u32 s41, s40, 0xc00
	s_add_i32 s41, s41, s39
	s_mulk_i32 s40, 0xc00
	s_waitcnt lgkmcnt(0)
	s_add_u32 s40, s6, s40
	s_addc_u32 s41, s7, s41
	s_ashr_i32 s39, s12, 31
	s_add_u32 s12, s12, s38
	s_addc_u32 s39, s39, 0
	s_mulk_i32 s39, 0xc00
	s_mul_hi_u32 s46, s12, 0xc00
	s_add_i32 s46, s46, s39
	s_mulk_i32 s12, 0xc00
	s_add_u32 s50, s6, s12
	s_addc_u32 s51, s7, s46
	s_ashr_i32 s12, s13, 31
	s_add_u32 s13, s13, s38
	s_addc_u32 s12, s12, 0
	s_mulk_i32 s12, 0xc00
	s_mul_hi_u32 s39, s13, 0xc00
	s_add_i32 s39, s39, s12
	s_mulk_i32 s13, 0xc00
	s_add_u32 s12, s6, s13
	s_addc_u32 s13, s7, s39
	s_ashr_i32 s39, s14, 31
	s_add_u32 s14, s14, s38
	v_lshlrev_b32_e32 v80, 4, v128
	s_addc_u32 s39, s39, 0
	global_load_dwordx4 v[22:25], v80, s[40:41]
	global_load_dwordx4 v[62:65], v80, s[40:41] offset:1024
	global_load_dwordx4 v[66:69], v80, s[40:41] offset:2048
	global_load_dwordx4 v[50:53], v80, s[50:51]
	global_load_dwordx4 v[54:57], v80, s[50:51] offset:1024
	global_load_dwordx4 v[58:61], v80, s[50:51] offset:2048
	s_mulk_i32 s39, 0xc00
	s_mul_hi_u32 s40, s14, 0xc00
	s_add_i32 s39, s40, s39
	s_mulk_i32 s14, 0xc00
	s_add_u32 s40, s6, s14
	global_load_dwordx4 v[38:41], v80, s[12:13]
	global_load_dwordx4 v[42:45], v80, s[12:13] offset:1024
	s_addc_u32 s41, s7, s39
	global_load_dwordx4 v[46:49], v80, s[12:13] offset:2048
	global_load_dwordx4 v[26:29], v80, s[40:41]
	global_load_dwordx4 v[30:33], v80, s[40:41] offset:1024
	global_load_dwordx4 v[34:37], v80, s[40:41] offset:2048
	s_mov_b32 s39, 0
	s_waitcnt vmcnt(12)
	ds_write_b128 v78, v[2:5]
	s_and_saveexec_b64 s[12:13], s[10:11]
	s_cbranch_execz .LBB5_75
	s_waitcnt vmcnt(12)
	ds_write_b128 v78, v[6:9] offset:10240

.LBB5_77:
	s_or_b64 exec, exec, s[12:13]
	s_and_saveexec_b64 s[12:13], s[4:5]
	s_cbranch_execz .LBB5_79
	s_waitcnt vmcnt(12)
	v_mov_b32_e32 v1, 0x23900
	v_mul_f32_e32 v14, v14, v86
	v_lshl_add_u32 v1, v0, 2, v1
	ds_write_b32 v1, v14

.LBB5_81:
	s_or_b64 exec, exec, s[12:13]
	s_and_saveexec_b64 s[12:13], s[2:3]
	s_cbranch_execz .LBB5_83
	s_waitcnt vmcnt(12)
	v_mov_b32_e32 v1, 0x22800
	v_pk_add_f32 v[12:13], v[12:13], v[18:19]
	v_pk_add_f32 v[10:11], v[10:11], v[16:17]
	v_lshl_add_u32 v1, v0, 4, v1
	ds_write_b128 v1, v[10:13]
.LBB5_83:
	s_or_b64 exec, exec, s[12:13]
	s_load_dwordx2 s[40:41], s[0:1], 0x78
	v_lshrrev_b32_e32 v126, 4, v128
	v_and_b32_e32 v127, 15, v0
	s_waitcnt vmcnt(12)
	v_mul_u32_u24_e32 v1, 48, v126
	s_waitcnt lgkmcnt(0)
	s_barrier
	v_or_b32_e32 v129, v1, v127
	s_mul_i32 s46, s45, 0xc00
	v_cmp_gt_u32_e64 s[2:3], 12, v127
	v_cndmask_b32_e64 v1, 0, 1, s[8:9]
	v_lshlrev_b32_e32 v131, 2, v126
	s_add_i32 s46, s46, 0x1b000
	v_mov_b32_e32 v71, 0
	v_cndmask_b32_e64 v130, 0, 1.0, s[2:3]
	v_cmp_ne_u32_e64 s[0:1], 1, v1
	s_andn2_b64 vcc, exec, s[8:9]
	v_add_u32_e32 v79, -8, v129
	v_mov_b32_e32 v70, 0
	s_cbranch_vccnz .LBB5_93
	v_cndmask_b32_e64 v1, v79, v129, s[2:3]
	v_lshlrev_b32_e32 v81, 2, v1
	v_add_u32_e32 v1, 0x22800, v81
	ds_read2_b32 v[6:7], v1 offset1:12
	ds_read2_b32 v[8:9], v1 offset0:24 offset1:36
	ds_read2_b32 v[10:11], v1 offset0:192 offset1:204
	ds_read2_b32 v[12:13], v1 offset0:216 offset1:228
	v_add_u32_e32 v2, 0x400, v1
	v_add_u32_e32 v1, 0x800, v1
	ds_read2_b32 v[14:15], v2 offset0:128 offset1:140
	ds_read2_b32 v[16:17], v2 offset0:152 offset1:164
	ds_read2_b32 v[70:71], v1 offset0:64 offset1:76
	ds_read_b128 v[2:5], v80
	ds_read2_b32 v[72:73], v1 offset0:88 offset1:100
	s_waitcnt lgkmcnt(0)
	v_cvt_pk_bf16_f32 v18, v6, v7
	v_cvt_pk_bf16_f32 v19, v8, v9
	ds_read_b128 v[6:9], v80 offset:1024
	v_cvt_pk_bf16_f32 v20, v10, v11
	v_cvt_pk_bf16_f32 v21, v12, v13
	ds_read_b128 v[10:13], v80 offset:2048
	v_cvt_pk_bf16_f32 v86, v14, v15
	v_mfma_f32_16x16x32_bf16 v[2:5], v[2:5], v[18:21], 0
	v_cvt_pk_bf16_f32 v87, v16, v17
	v_cvt_pk_bf16_f32 v88, v70, v71
	v_cvt_pk_bf16_f32 v89, v72, v73
	ds_read_b128 v[70:73], v80 offset:4096
	v_mov_b32_e32 v1, 0x23e00
	s_waitcnt lgkmcnt(2)
	v_mfma_f32_16x16x32_bf16 v[14:17], v[6:9], v[86:89], v[2:5]
	v_add_u32_e32 v96, s46, v81
	s_cmp_lt_i32 s48, 1
	ds_read_b128 v[74:77], v80 offset:6144
	ds_read_b128 v[2:5], v80 offset:3072
	s_waitcnt lgkmcnt(3)
	v_mfma_f32_16x16x32_bf16 v[6:9], v[10:13], v[18:21], 0
	s_mov_b32 s8, 0x43998000
	s_waitcnt lgkmcnt(0)
	v_mfma_f32_16x16x32_bf16 v[10:13], v[2:5], v[86:89], v[6:9]
	ds_read_b128 v[2:5], v80 offset:5120
	v_mfma_f32_16x16x32_bf16 v[6:9], v[70:73], v[18:21], 0
	ds_read_b128 v[70:73], v80 offset:7168
	s_waitcnt lgkmcnt(1)
	v_mfma_f32_16x16x32_bf16 v[6:9], v[2:5], v[86:89], v[6:9]
	v_mfma_f32_16x16x32_bf16 v[2:5], v[74:77], v[18:21], 0
	v_mov_b32_e32 v18, 0x23e10
	ds_read_b128 v[98:101], v1
	ds_read_b128 v[18:21], v18
	v_add_u32_e32 v1, s46, v80
	s_waitcnt vmcnt(11)
	ds_write_b128 v1, v[22:25]
	s_waitcnt vmcnt(10)
	ds_write_b128 v1, v[62:65] offset:1024
	s_waitcnt vmcnt(9)
	ds_write_b128 v1, v[66:69] offset:2048
	s_waitcnt lgkmcnt(5)
	v_mfma_f32_16x16x32_bf16 v[2:5], v[70:73], v[86:89], v[2:5]
	ds_read2_b32 v[88:89], v96 offset1:12
	ds_read2_b32 v[90:91], v96 offset0:24 offset1:36
	ds_read2_b32 v[86:87], v96 offset0:192 offset1:204
	ds_read2_b32 v[82:83], v96 offset0:216 offset1:228
	v_add_u32_e32 v63, 0x400, v96
	ds_read2_b32 v[66:67], v63 offset0:128 offset1:140
	ds_read2_b32 v[68:69], v63 offset0:152 offset1:164
	v_add_u32_e32 v62, 0x800, v96
	ds_read_b128 v[22:25], v80 offset:8192
	ds_read2_b32 v[94:95], v62 offset0:64 offset1:76
	ds_read2_b32 v[92:93], v62 offset0:88 offset1:100
	ds_read_b128 v[106:109], v80 offset:9216
	s_waitcnt lgkmcnt(9)
	v_cvt_pk_bf16_f32 v102, v88, v89
	s_waitcnt lgkmcnt(8)
	v_cvt_pk_bf16_f32 v103, v90, v91
	s_waitcnt lgkmcnt(7)
	v_cvt_pk_bf16_f32 v104, v86, v87
	s_waitcnt lgkmcnt(6)
	v_cvt_pk_bf16_f32 v105, v82, v83
	s_waitcnt lgkmcnt(5)
	v_cvt_pk_bf16_f32 v110, v66, v67
	s_waitcnt lgkmcnt(4)
	v_cvt_pk_bf16_f32 v111, v68, v69
	s_waitcnt lgkmcnt(3)
	v_mfma_f32_16x16x32_bf16 v[22:25], v[22:25], v[102:105], v[98:101]
	s_waitcnt lgkmcnt(2)
	v_cvt_pk_bf16_f32 v112, v94, v95
	s_waitcnt lgkmcnt(1)
	v_cvt_pk_bf16_f32 v113, v92, v93
	s_waitcnt lgkmcnt(0)
	s_nop 0
	v_mfma_f32_16x16x32_bf16 v[22:25], v[106:109], v[110:113], v[22:25]
	v_min_u32_e32 v133, 47, v128
	s_mul_i32 s58, s37, 0xc00
	v_lshlrev_b32_e32 v133, 6, v133
	v_add_u32_e32 v133, s58, v133
	global_load_dword v134, v133, s[28:29]
	global_load_dword v135, v133, s[30:31]
	s_cbranch_scc1 .LBB5_209
	s_waitcnt vmcnt(10)
	ds_write_b128 v1, v[50:53]
	s_waitcnt vmcnt(9)
	ds_write_b128 v1, v[54:57] offset:1024
	s_waitcnt vmcnt(8)
	ds_write_b128 v1, v[58:61] offset:2048
	ds_read2_b32 v[54:55], v96 offset1:12
	ds_read2_b32 v[56:57], v96 offset0:24 offset1:36
	ds_read2_b32 v[64:65], v96 offset0:192 offset1:204
	ds_read2_b32 v[98:99], v96 offset0:216 offset1:228
	ds_read2_b32 v[100:101], v63 offset0:128 offset1:140
	ds_read2_b32 v[102:103], v63 offset0:152 offset1:164
	ds_read2_b32 v[104:105], v62 offset0:64 offset1:76
	ds_read_b128 v[50:53], v80
	ds_read2_b32 v[106:107], v62 offset0:88 offset1:100
	ds_read_b128 v[58:61], v80 offset:1024
	s_waitcnt lgkmcnt(9)
	v_cvt_pk_bf16_f32 v54, v54, v55
	s_waitcnt lgkmcnt(8)
	v_cvt_pk_bf16_f32 v55, v56, v57
	s_waitcnt lgkmcnt(7)
	v_cvt_pk_bf16_f32 v56, v64, v65
	s_waitcnt lgkmcnt(6)
	v_cvt_pk_bf16_f32 v57, v98, v99
	s_waitcnt lgkmcnt(5)
	v_cvt_pk_bf16_f32 v62, v100, v101
	ds_read_b128 v[98:101], v80 offset:2048
	s_waitcnt lgkmcnt(3)
	v_mfma_f32_16x16x32_bf16 v[50:53], v[50:53], v[54:57], 0
	v_cvt_pk_bf16_f32 v63, v102, v103
	v_cvt_pk_bf16_f32 v64, v104, v105
	s_waitcnt lgkmcnt(2)
	v_cvt_pk_bf16_f32 v65, v106, v107
	s_waitcnt lgkmcnt(0)
	v_mfma_f32_16x16x32_bf16 v[98:101], v[98:101], v[54:57], 0
	ds_read_b128 v[102:105], v80 offset:4096
	ds_read_b128 v[106:109], v80 offset:11264
	v_mfma_f32_16x16x32_bf16 v[50:53], v[58:61], v[62:65], v[50:53]
	ds_read_b128 v[58:61], v80 offset:3072
	s_waitcnt lgkmcnt(0)
	v_mfma_f32_16x16x32_bf16 v[58:61], v[58:61], v[62:65], v[98:101]
	s_nop 2
	ds_read_b128 v[98:101], v80 offset:5120
	v_mfma_f32_16x16x32_bf16 v[102:105], v[102:105], v[54:57], 0
	s_waitcnt lgkmcnt(0)
	v_mfma_f32_16x16x32_bf16 v[98:101], v[98:101], v[62:65], v[102:105]
	s_nop 5
	ds_read_b128 v[102:105], v80 offset:10240
	v_mfma_f32_16x16x32_bf16 v[74:77], v[74:77], v[54:57], 0
	s_waitcnt lgkmcnt(0)
	v_mfma_f32_16x16x32_bf16 v[54:57], v[102:105], v[54:57], v[18:21]
	v_mfma_f32_16x16x32_bf16 v[54:57], v[106:109], v[62:65], v[54:57]
	v_mfma_f32_16x16x32_bf16 v[62:65], v[70:73], v[62:65], v[74:77]
	s_nop 6
	v_add_f32_e32 v54, v22, v54
	v_mul_f32_e32 v81, 0x3e4ccccd, v54
	v_cmp_lt_f32_e32 vcc, 0, v54
	v_add_f32_e32 v55, v23, v55
	v_mul_f32_e32 v97, 0x3e4ccccd, v55
	v_cndmask_b32_e32 v54, v81, v54, vcc
	v_cmp_lt_f32_e32 vcc, 0, v55
	v_mov_b32_e32 v81, s18
	v_fma_f32 v54, s15, v54, v81
	v_cndmask_b32_e32 v55, v97, v55, vcc
	v_fma_f32 v55, s15, v55, v81
	v_mul_f32_e32 v54, 0x3fb8aa3b, v54
	v_mul_f32_e32 v55, 0x3fb8aa3b, v55
	v_exp_f32_e32 v54, v54
	v_exp_f32_e32 v55, v55
	s_nop 0
	v_pk_add_f32 v[54:55], v[54:55], -1.0 op_sel_hi:[1,0]
	s_nop 0
	v_pk_fma_f32 v[16:17], v[52:53], v[54:55], v[16:17] op_sel_hi:[1,0,1]
	v_add_f32_e32 v52, v24, v56
	v_mul_f32_e32 v53, 0x3e4ccccd, v52
	v_cmp_lt_f32_e32 vcc, 0, v52
	v_pk_fma_f32 v[14:15], v[50:51], v[54:55], v[14:15] op_sel_hi:[1,0,1]
	v_pk_fma_f32 v[12:13], v[60:61], v[54:55], v[12:13] op_sel:[0,1,0]
	v_cndmask_b32_e32 v52, v53, v52, vcc
	v_add_f32_e32 v53, v25, v57
	v_mul_f32_e32 v56, 0x3e4ccccd, v53
	v_cmp_lt_f32_e32 vcc, 0, v53
	v_fma_f32 v52, s15, v52, v81
	v_mul_f32_e32 v52, 0x3fb8aa3b, v52
	v_cndmask_b32_e32 v53, v56, v53, vcc
	v_fma_f32 v53, s15, v53, v81
	v_mul_f32_e32 v53, 0x3fb8aa3b, v53
	v_exp_f32_e32 v52, v52
	v_exp_f32_e32 v53, v53
	v_pk_fma_f32 v[10:11], v[58:59], v[54:55], v[10:11] op_sel:[0,1,0]
	v_pk_add_f32 v[72:73], v[54:55], s[8:9] op_sel_hi:[1,0]
	v_pk_add_f32 v[50:51], v[52:53], -1.0 op_sel_hi:[1,0]
	s_nop 0
	v_pk_fma_f32 v[8:9], v[100:101], v[50:51], v[8:9] op_sel_hi:[1,0,1]
	v_pk_fma_f32 v[6:7], v[98:99], v[50:51], v[6:7] op_sel_hi:[1,0,1]
	v_pk_add_f32 v[70:71], v[50:51], s[8:9] op_sel_hi:[1,0]
	v_pk_fma_f32 v[4:5], v[64:65], v[50:51], v[4:5] op_sel:[0,1,0]
	v_pk_fma_f32 v[2:3], v[62:63], v[50:51], v[2:3] op_sel:[0,1,0]
	s_cmp_lt_i32 s48, 2
	s_cbranch_scc1 .LBB5_87
.LBB5_86:
	s_waitcnt vmcnt(7)
	ds_write_b128 v1, v[38:41]
	s_waitcnt vmcnt(6)
	ds_write_b128 v1, v[42:45] offset:1024
	s_waitcnt vmcnt(5)
	ds_write_b128 v1, v[46:49] offset:2048
	ds_read2_b32 v[42:43], v96 offset1:12
	ds_read2_b32 v[44:45], v96 offset0:24 offset1:36
	ds_read2_b32 v[50:51], v96 offset0:192 offset1:204
	ds_read2_b32 v[52:53], v96 offset0:216 offset1:228
	v_add_u32_e32 v38, 0x400, v96
	v_add_u32_e32 v46, 0x800, v96
	ds_read2_b32 v[54:55], v38 offset0:128 offset1:140
	ds_read2_b32 v[58:59], v38 offset0:152 offset1:164
	ds_read2_b32 v[60:61], v46 offset0:64 offset1:76
	ds_read_b128 v[38:41], v80
	ds_read2_b32 v[62:63], v46 offset0:88 offset1:100
	ds_read_b128 v[46:49], v80 offset:1024
	s_waitcnt lgkmcnt(9)
	v_cvt_pk_bf16_f32 v42, v42, v43
	s_waitcnt lgkmcnt(8)
	v_cvt_pk_bf16_f32 v43, v44, v45
	s_waitcnt lgkmcnt(7)
	v_cvt_pk_bf16_f32 v44, v50, v51
	s_waitcnt lgkmcnt(6)
	v_cvt_pk_bf16_f32 v45, v52, v53
	s_waitcnt lgkmcnt(5)
	v_cvt_pk_bf16_f32 v50, v54, v55
	ds_read_b128 v[54:57], v80 offset:2048
	s_waitcnt lgkmcnt(3)
	v_mfma_f32_16x16x32_bf16 v[38:41], v[38:41], v[42:45], 0
	v_cvt_pk_bf16_f32 v51, v58, v59
	v_cvt_pk_bf16_f32 v52, v60, v61
	s_waitcnt lgkmcnt(2)
	v_cvt_pk_bf16_f32 v53, v62, v63
	s_waitcnt lgkmcnt(0)
	v_mfma_f32_16x16x32_bf16 v[54:57], v[54:57], v[42:45], 0
	ds_read_b128 v[58:61], v80 offset:4096
	ds_read_b128 v[62:65], v80 offset:6144
	v_mfma_f32_16x16x32_bf16 v[38:41], v[46:49], v[50:53], v[38:41]
	ds_read_b128 v[46:49], v80 offset:3072
	s_waitcnt lgkmcnt(0)
	v_mfma_f32_16x16x32_bf16 v[46:49], v[46:49], v[50:53], v[54:57]
	s_nop 2
	ds_read_b128 v[54:57], v80 offset:5120
	v_mfma_f32_16x16x32_bf16 v[58:61], v[58:61], v[42:45], 0
	s_waitcnt lgkmcnt(0)
	v_mfma_f32_16x16x32_bf16 v[54:57], v[54:57], v[50:53], v[58:61]
	s_nop 5
	ds_read_b128 v[58:61], v80 offset:10240
	ds_read_b128 v[74:77], v80 offset:7168
	ds_read_b128 v[98:101], v80 offset:11264
	v_mfma_f32_16x16x32_bf16 v[62:65], v[62:65], v[42:45], 0
	s_waitcnt lgkmcnt(2)
	v_mfma_f32_16x16x32_bf16 v[42:45], v[58:61], v[42:45], v[18:21]
	s_waitcnt lgkmcnt(0)
	v_mfma_f32_16x16x32_bf16 v[42:45], v[98:101], v[50:53], v[42:45]
	v_mfma_f32_16x16x32_bf16 v[50:53], v[74:77], v[50:53], v[62:65]
	s_nop 6
	v_add_f32_e32 v42, v22, v42
	v_mul_f32_e32 v58, 0x3e4ccccd, v42
	v_cmp_lt_f32_e32 vcc, 0, v42
	v_add_f32_e32 v43, v23, v43
	v_mul_f32_e32 v59, 0x3e4ccccd, v43
	v_cndmask_b32_e32 v42, v58, v42, vcc
	v_cmp_lt_f32_e32 vcc, 0, v43
	v_mov_b32_e32 v58, s19
	v_fma_f32 v42, s16, v42, v58
	v_cndmask_b32_e32 v43, v59, v43, vcc
	v_fma_f32 v43, s16, v43, v58
	v_mul_f32_e32 v42, 0x3fb8aa3b, v42
	v_mul_f32_e32 v43, 0x3fb8aa3b, v43
	v_exp_f32_e32 v42, v42
	v_exp_f32_e32 v43, v43
	s_nop 0
	v_pk_add_f32 v[42:43], v[42:43], -1.0 op_sel_hi:[1,0]
	s_nop 0
	v_pk_fma_f32 v[16:17], v[40:41], v[42:43], v[16:17] op_sel_hi:[1,0,1]
	v_add_f32_e32 v40, v24, v44
	v_mul_f32_e32 v41, 0x3e4ccccd, v40
	v_cmp_lt_f32_e32 vcc, 0, v40
	v_pk_fma_f32 v[14:15], v[38:39], v[42:43], v[14:15] op_sel_hi:[1,0,1]
	v_pk_fma_f32 v[12:13], v[48:49], v[42:43], v[12:13] op_sel:[0,1,0]
	v_cndmask_b32_e32 v40, v41, v40, vcc
	v_add_f32_e32 v41, v25, v45
	v_mul_f32_e32 v44, 0x3e4ccccd, v41
	v_cmp_lt_f32_e32 vcc, 0, v41
	v_fma_f32 v40, s16, v40, v58
	v_mul_f32_e32 v40, 0x3fb8aa3b, v40
	v_cndmask_b32_e32 v41, v44, v41, vcc
	v_fma_f32 v41, s16, v41, v58
	v_mul_f32_e32 v41, 0x3fb8aa3b, v41
	v_exp_f32_e32 v40, v40
	v_exp_f32_e32 v41, v41
	v_pk_fma_f32 v[10:11], v[46:47], v[42:43], v[10:11] op_sel:[0,1,0]
	v_pk_add_f32 v[72:73], v[72:73], v[42:43]
	v_pk_add_f32 v[38:39], v[40:41], -1.0 op_sel_hi:[1,0]
	s_nop 0
	v_pk_fma_f32 v[8:9], v[56:57], v[38:39], v[8:9] op_sel_hi:[1,0,1]
	v_pk_fma_f32 v[6:7], v[54:55], v[38:39], v[6:7] op_sel_hi:[1,0,1]
	v_pk_add_f32 v[70:71], v[70:71], v[38:39]
	v_pk_fma_f32 v[4:5], v[52:53], v[38:39], v[4:5] op_sel:[0,1,0]
	v_pk_fma_f32 v[2:3], v[50:51], v[38:39], v[2:3] op_sel:[0,1,0]
.LBB5_87:
	s_cmp_lt_i32 s48, 3
	s_cbranch_scc1 .LBB5_89
	s_waitcnt vmcnt(4)
	ds_write_b128 v1, v[26:29]
	s_waitcnt vmcnt(3)
	ds_write_b128 v1, v[30:33] offset:1024
	s_waitcnt vmcnt(2)
	ds_write_b128 v1, v[34:37] offset:2048
	ds_read2_b32 v[30:31], v96 offset1:12
	ds_read2_b32 v[32:33], v96 offset0:24 offset1:36
	ds_read2_b32 v[38:39], v96 offset0:192 offset1:204
	ds_read2_b32 v[40:41], v96 offset0:216 offset1:228
	v_add_u32_e32 v26, 0x400, v96
	v_add_u32_e32 v34, 0x800, v96
	ds_read2_b32 v[42:43], v26 offset0:128 offset1:140
	ds_read2_b32 v[46:47], v26 offset0:152 offset1:164
	ds_read2_b32 v[48:49], v34 offset0:64 offset1:76
	ds_read_b128 v[26:29], v80
	ds_read2_b32 v[50:51], v34 offset0:88 offset1:100
	ds_read_b128 v[34:37], v80 offset:1024
	s_waitcnt lgkmcnt(9)
	v_cvt_pk_bf16_f32 v30, v30, v31
	s_waitcnt lgkmcnt(8)
	v_cvt_pk_bf16_f32 v31, v32, v33
	s_waitcnt lgkmcnt(7)
	v_cvt_pk_bf16_f32 v32, v38, v39
	s_waitcnt lgkmcnt(6)
	v_cvt_pk_bf16_f32 v33, v40, v41
	s_waitcnt lgkmcnt(5)
	v_cvt_pk_bf16_f32 v38, v42, v43
	ds_read_b128 v[42:45], v80 offset:2048
	s_waitcnt lgkmcnt(3)
	v_mfma_f32_16x16x32_bf16 v[26:29], v[26:29], v[30:33], 0
	v_cvt_pk_bf16_f32 v39, v46, v47
	v_cvt_pk_bf16_f32 v40, v48, v49
	s_waitcnt lgkmcnt(2)
	v_cvt_pk_bf16_f32 v41, v50, v51
	s_waitcnt lgkmcnt(0)
	v_mfma_f32_16x16x32_bf16 v[42:45], v[42:45], v[30:33], 0
	ds_read_b128 v[46:49], v80 offset:4096
	ds_read_b128 v[50:53], v80 offset:6144
	v_mfma_f32_16x16x32_bf16 v[26:29], v[34:37], v[38:41], v[26:29]
	ds_read_b128 v[34:37], v80 offset:3072
	s_waitcnt lgkmcnt(0)
	v_mfma_f32_16x16x32_bf16 v[34:37], v[34:37], v[38:41], v[42:45]
	s_nop 2
	ds_read_b128 v[42:45], v80 offset:5120
	v_mfma_f32_16x16x32_bf16 v[46:49], v[46:49], v[30:33], 0
	s_waitcnt lgkmcnt(0)
	v_mfma_f32_16x16x32_bf16 v[42:45], v[42:45], v[38:41], v[46:49]
	s_nop 5
	ds_read_b128 v[46:49], v80 offset:10240
	ds_read_b128 v[54:57], v80 offset:7168
	ds_read_b128 v[58:61], v80 offset:11264
	v_mfma_f32_16x16x32_bf16 v[50:53], v[50:53], v[30:33], 0
	s_waitcnt lgkmcnt(2)
	v_mfma_f32_16x16x32_bf16 v[30:33], v[46:49], v[30:33], v[18:21]
	s_waitcnt lgkmcnt(0)
	v_mfma_f32_16x16x32_bf16 v[30:33], v[58:61], v[38:41], v[30:33]
	v_mfma_f32_16x16x32_bf16 v[38:41], v[54:57], v[38:41], v[50:53]
	s_nop 6
	v_add_f32_e32 v30, v22, v30
	v_mul_f32_e32 v46, 0x3e4ccccd, v30
	v_cmp_lt_f32_e32 vcc, 0, v30
	v_add_f32_e32 v31, v23, v31
	v_mul_f32_e32 v47, 0x3e4ccccd, v31
	v_cndmask_b32_e32 v30, v46, v30, vcc
	v_cmp_lt_f32_e32 vcc, 0, v31
	v_mov_b32_e32 v46, s49
	v_fma_f32 v30, s17, v30, v46
	v_cndmask_b32_e32 v31, v47, v31, vcc
	v_fma_f32 v31, s17, v31, v46
	v_mul_f32_e32 v30, 0x3fb8aa3b, v30
	v_mul_f32_e32 v31, 0x3fb8aa3b, v31
	v_exp_f32_e32 v30, v30
	v_exp_f32_e32 v31, v31
	s_nop 0
	v_pk_add_f32 v[30:31], v[30:31], -1.0 op_sel_hi:[1,0]
	s_nop 0
	v_pk_fma_f32 v[16:17], v[28:29], v[30:31], v[16:17] op_sel_hi:[1,0,1]
	v_add_f32_e32 v28, v24, v32
	v_mul_f32_e32 v29, 0x3e4ccccd, v28
	v_cmp_lt_f32_e32 vcc, 0, v28
	v_pk_fma_f32 v[14:15], v[26:27], v[30:31], v[14:15] op_sel_hi:[1,0,1]
	v_pk_fma_f32 v[12:13], v[36:37], v[30:31], v[12:13] op_sel:[0,1,0]
	v_cndmask_b32_e32 v28, v29, v28, vcc
	v_add_f32_e32 v29, v25, v33
	v_mul_f32_e32 v32, 0x3e4ccccd, v29
	v_cmp_lt_f32_e32 vcc, 0, v29
	v_fma_f32 v28, s17, v28, v46
	v_mul_f32_e32 v28, 0x3fb8aa3b, v28
	v_cndmask_b32_e32 v29, v32, v29, vcc
	v_fmac_f32_e32 v46, s17, v29
	v_mul_f32_e32 v29, 0x3fb8aa3b, v46
	v_exp_f32_e32 v28, v28
	v_exp_f32_e32 v29, v29
	v_pk_fma_f32 v[10:11], v[34:35], v[30:31], v[10:11] op_sel:[0,1,0]
	v_pk_add_f32 v[72:73], v[72:73], v[30:31]
	v_pk_add_f32 v[26:27], v[28:29], -1.0 op_sel_hi:[1,0]
	s_nop 0
	v_pk_fma_f32 v[8:9], v[44:45], v[26:27], v[8:9] op_sel_hi:[1,0,1]
	v_pk_fma_f32 v[6:7], v[42:43], v[26:27], v[6:7] op_sel_hi:[1,0,1]
	v_pk_add_f32 v[70:71], v[70:71], v[26:27]
	v_pk_fma_f32 v[4:5], v[40:41], v[26:27], v[4:5] op_sel:[0,1,0]
	v_pk_fma_f32 v[2:3], v[38:39], v[26:27], v[2:3] op_sel:[0,1,0]
	s_cmp_lt_i32 s48, 4
	s_cbranch_scc1 .LBB5_92
	s_branch .LBB5_90

.LBB5_92:
	v_lshlrev_b32_e32 v1, 2, v131
	v_or_b32_e32 v18, 0x23d00, v1
	v_or_b32_e32 v22, 0x23d40, v1
	ds_read_b128 v[18:21], v18
	ds_read_b128 v[22:25], v22
	s_waitcnt vmcnt(4)
	v_rcp_f32_e32 v26, v72
	v_rcp_f32_e32 v28, v73
	s_waitcnt lgkmcnt(1)
	v_pk_fma_f32 v[14:15], v[26:27], v[14:15], v[18:19] op_sel_hi:[0,1,1]
	s_waitcnt lgkmcnt(0)
	v_pk_fma_f32 v[10:11], v[28:29], v[10:11], v[22:23] op_sel_hi:[0,1,1]
	v_pk_add_f32 v[120:121], v[14:15], v[88:89]
	v_pk_fma_f32 v[14:15], v[26:27], v[16:17], v[20:21] op_sel_hi:[0,1,1]
	v_pk_add_f32 v[118:119], v[10:11], v[86:87]
	v_or_b32_e32 v10, 0x23d80, v1
	v_pk_add_f32 v[122:123], v[14:15], v[90:91]
	v_pk_fma_f32 v[14:15], v[28:29], v[12:13], v[24:25] op_sel_hi:[0,1,1]
	ds_read_b128 v[10:13], v10
	v_rcp_f32_e32 v18, v70
	v_or_b32_e32 v1, 0x23dc0, v1
	v_pk_add_f32 v[124:125], v[14:15], v[82:83]
	ds_read_b128 v[14:17], v1
	s_waitcnt lgkmcnt(1)
	v_pk_fma_f32 v[6:7], v[18:19], v[6:7], v[10:11] op_sel_hi:[0,1,1]
	v_rcp_f32_e32 v10, v71
	v_pk_add_f32 v[116:117], v[6:7], v[66:67]
	v_pk_fma_f32 v[6:7], v[18:19], v[8:9], v[12:13] op_sel_hi:[0,1,1]
	v_pk_add_f32 v[114:115], v[6:7], v[68:69]
	s_waitcnt lgkmcnt(0)
	v_pk_fma_f32 v[2:3], v[10:11], v[2:3], v[14:15] op_sel_hi:[0,1,1]
	v_pk_add_f32 v[110:111], v[2:3], v[94:95]
	v_pk_fma_f32 v[2:3], v[10:11], v[4:5], v[16:17] op_sel_hi:[0,1,1]
	v_pk_add_f32 v[112:113], v[2:3], v[92:93]
	v_mul_f32_e32 v3, v130, v120
	v_mul_f32_e32 v2, v120, v3
	v_mul_f32_e32 v5, v130, v121
	v_pk_add_f32 v[2:3], v[2:3], 0 op_sel_hi:[1,0]
	v_mul_f32_e32 v4, v121, v5
	v_pk_add_f32 v[2:3], v[2:3], v[4:5]
	v_mul_f32_e32 v5, v130, v122
	v_mul_f32_e32 v4, v122, v5
	v_pk_add_f32 v[2:3], v[2:3], v[4:5]
	v_mul_f32_e32 v5, v130, v123
	v_mul_f32_e32 v4, v123, v5
	v_pk_add_f32 v[2:3], v[2:3], v[4:5]
	v_mul_f32_e32 v5, v130, v118
	v_mul_f32_e32 v4, v118, v5
	v_pk_add_f32 v[2:3], v[2:3], v[4:5]
	v_mul_f32_e32 v5, v130, v119
	v_mul_f32_e32 v4, v119, v5
	v_mul_f32_e32 v7, v130, v124
	v_mul_f32_e32 v6, v124, v7
	v_mul_f32_e32 v9, v130, v125
	v_pk_add_f32 v[2:3], v[2:3], v[4:5]
	v_mul_f32_e32 v8, v125, v9
	v_mul_f32_e32 v11, v130, v116
	v_pk_add_f32 v[2:3], v[2:3], v[6:7]
	v_mul_f32_e32 v10, v116, v11
	v_mul_f32_e32 v13, v130, v117
	v_pk_add_f32 v[2:3], v[2:3], v[8:9]
	v_mul_f32_e32 v12, v117, v13
	v_mul_f32_e32 v15, v130, v114
	v_pk_add_f32 v[2:3], v[2:3], v[10:11]
	v_mul_f32_e32 v14, v114, v15
	v_mul_f32_e32 v17, v130, v115
	v_pk_add_f32 v[2:3], v[2:3], v[12:13]
	v_mul_f32_e32 v16, v115, v17
	v_mul_f32_e32 v19, v130, v110
	v_pk_add_f32 v[2:3], v[2:3], v[14:15]
	v_mul_f32_e32 v18, v110, v19
	v_mul_f32_e32 v21, v130, v111
	v_pk_add_f32 v[2:3], v[2:3], v[16:17]
	v_mul_f32_e32 v20, v111, v21
	v_mul_f32_e32 v23, v130, v112
	v_pk_add_f32 v[2:3], v[2:3], v[18:19]
	v_mul_f32_e32 v22, v112, v23
	v_pk_add_f32 v[2:3], v[2:3], v[20:21]
	v_mul_f32_e32 v5, v130, v113
	v_pk_add_f32 v[2:3], v[2:3], v[22:23]
	v_mul_f32_e32 v4, v113, v5
	v_pk_add_f32 v[70:71], v[2:3], v[4:5]

.LBB5_130:
	v_add_co_u32_e32 v10, vcc, 0xb000, v84
	v_or_b32_e32 v1, 0x1000, v0
	s_nop 0
	v_addc_co_u32_e32 v11, vcc, 0, v85, vcc
	v_add_co_u32_e32 v12, vcc, 0xd000, v84
	v_lshlrev_b32_e32 v83, 4, v1
	s_nop 0
	v_addc_co_u32_e32 v13, vcc, 0, v85, vcc
	v_add_co_u32_e32 v18, vcc, 0x12000, v84
	s_waitcnt lgkmcnt(0)
	s_nop 0
	v_addc_co_u32_e32 v19, vcc, 0, v85, vcc
	s_barrier
	v_min_u32_e32 v154, 47, v128
	v_lshlrev_b32_e32 v154, 6, v154
	v_add_u32_e32 v154, s14, v154
	global_load_dword v155, v154, s[24:25]
	global_load_dword v156, v154, s[26:27]
	global_load_dword v157, v154, s[20:21]
	global_load_dword v158, v154, s[22:23]
	global_load_dwordx4 v[2:5], v[10:11], off
	global_load_dwordx4 v[6:9], v[12:13], off offset:2048
	s_nop 0
	global_load_dwordx4 v[10:13], v83, s[42:43]
	global_load_dwordx4 v[14:17], v[18:19], off offset:2048
	v_add_co_u32_e32 v18, vcc, 0x15000, v84
	s_movk_i32 s10, 0x380
	s_nop 0
	v_addc_co_u32_e32 v19, vcc, 0, v85, vcc
	global_load_dwordx4 v[22:25], v[18:19], off
	v_cmp_gt_u32_e64 s[10:11], s10, v0
	s_and_saveexec_b64 s[12:13], s[10:11]
	s_cbranch_execz .LBB5_132
	v_add_co_u32_e32 v0, vcc, 0x17000, v84
	s_nop 1
	v_addc_co_u32_e32 v1, vcc, 0, v85, vcc
	global_load_dwordx4 v[18:21], v[0:1], off offset:2048
